# baseline (speedup 1.0000x reference)
.LBB0_33:
	s_mov_b32 s91, 2
